# speedup vs baseline: 1.0161x; 1.0161x over previous
.Lfast2:
	v_mfma_f32_16x16x32_f16 v[6:9], a[16:19], v[240:243], v[6:9]
	v_and_b32_dpp v244, v70, v167 row_ror:8 row_mask:0xf bank_mask:0xf
	v_and_b32_dpp v245, v71, v167 row_ror:8 row_mask:0xf bank_mask:0xf
	v_mfma_f32_16x16x32_f16 v[10:13], a[48:51], v[240:243], v[10:13]
	v_and_b32_dpp v246, v72, v167 row_ror:8 row_mask:0xf bank_mask:0xf
	v_and_b32_dpp v247, v73, v167 row_ror:8 row_mask:0xf bank_mask:0xf
	v_mfma_f32_16x16x32_f16 v[14:17], a[80:83], v[240:243], v[14:17]
	ds_read_b128 v[162:165], v222 offset:8192
	ds_read_b128 v[158:161], v222 offset:9216
	v_mfma_f32_16x16x32_f16 v[18:21], a[112:115], v[240:243], v[18:21]
	ds_read_b128 v[154:157], v222 offset:10240
	ds_read_b128 v[150:153], v222 offset:11264
	v_mfma_f32_16x16x32_f16 v[22:25], a[144:147], v[240:243], v[22:25]
	s_waitcnt vmcnt(0)
	v_mfma_f32_16x16x32_f16 v[26:29], a[176:179], v[240:243], v[26:29]
	v_bitop3_b32 v168, v74, v75, s30 bitop3:0x7e
	v_bitop3_b32 v169, v76, v77, s30 bitop3:0x7e
	v_mfma_f32_16x16x32_f16 v[30:33], a[208:211], v[240:243], v[30:33]
	v_bitop3_b32 v168, v168, v169, s18 bitop3:0xa8
	v_cmp_ne_u32_e32 vcc, 0, v168
	v_mfma_f32_16x16x32_f16 v[34:37], a[240:243], v[240:243], v[34:37]
	v_and_b32_e32 v248, v74, v167
	v_and_b32_e32 v249, v75, v167
	v_mfma_f32_16x16x32_f16 v[6:9], a[20:23], v[244:247], v[6:9]
	v_and_b32_e32 v250, v76, v167
	v_and_b32_e32 v251, v77, v167
	v_mfma_f32_16x16x32_f16 v[10:13], a[52:55], v[244:247], v[10:13]
	ds_read_b128 v[146:149], v222 offset:12288
	ds_read_b128 v[142:145], v222 offset:13312
	v_mfma_f32_16x16x32_f16 v[14:17], a[84:87], v[244:247], v[14:17]
	ds_read_b128 v[138:141], v222 offset:14336
	ds_read_b128 v[134:137], v222 offset:15360
	v_mfma_f32_16x16x32_f16 v[18:21], a[116:119], v[244:247], v[18:21]
	v_and_b32_dpp v252, v74, v167 row_ror:8 row_mask:0xf bank_mask:0xf
	v_and_b32_dpp v253, v75, v167 row_ror:8 row_mask:0xf bank_mask:0xf
	v_mfma_f32_16x16x32_f16 v[22:25], a[148:151], v[244:247], v[22:25]
	v_and_b32_dpp v254, v76, v167 row_ror:8 row_mask:0xf bank_mask:0xf
	v_and_b32_dpp v255, v77, v167 row_ror:8 row_mask:0xf bank_mask:0xf
	v_mfma_f32_16x16x32_f16 v[26:29], a[180:183], v[244:247], v[26:29]
	v_mfma_f32_16x16x32_f16 v[30:33], a[212:215], v[244:247], v[30:33]
	v_mfma_f32_16x16x32_f16 v[34:37], a[244:247], v[244:247], v[34:37]
	s_cbranch_vccnz .Lrestart3
.Lfast3:
	v_mfma_f32_16x16x32_f16 v[6:9], a[24:27], v[248:251], v[6:9]
	global_load_dwordx4 v[46:49], v[4:5], off
	v_mfma_f32_16x16x32_f16 v[6:9], a[28:31], v[252:255], v[6:9]
	global_load_dwordx4 v[50:53], v[4:5], off offset:16
	v_mfma_f32_16x16x32_f16 v[10:13], a[56:59], v[248:251], v[10:13]
	global_load_dwordx4 v[38:41], v[4:5], off offset:128
	v_mfma_f32_16x16x32_f16 v[10:13], a[60:63], v[252:255], v[10:13]
	global_load_dwordx4 v[42:45], v[4:5], off offset:144
	v_mfma_f32_16x16x32_f16 v[14:17], a[88:91], v[248:251], v[14:17]
	s_cmp_lg_u32 s31, 0
	s_cbranch_scc1 .Lno_warm
	global_load_dwordx4 v[54:57], v[172:173], off
	global_load_dwordx4 v[58:61], v[172:173], off offset:1024
.Lno_warm:
	v_mfma_f32_16x16x32_f16 v[14:17], a[92:95], v[252:255], v[14:17]
	v_mfma_f32_16x16x32_f16 v[18:21], a[120:123], v[248:251], v[18:21]
	v_mfma_f32_16x16x32_f16 v[18:21], a[124:127], v[252:255], v[18:21]
	v_mfma_f32_16x16x32_f16 v[22:25], a[152:155], v[248:251], v[22:25]
	v_mfma_f32_16x16x32_f16 v[22:25], a[156:159], v[252:255], v[22:25]
	s_mov_b64 exec, s[2:3]
	ds_write_b128 v174, v[6:9]
	v_mfma_f32_16x16x32_f16 v[26:29], a[184:187], v[248:251], v[26:29]
	v_mfma_f32_16x16x32_f16 v[26:29], a[188:191], v[252:255], v[26:29]
	ds_write_b128 v174, v[10:13] offset:512
	v_mfma_f32_16x16x32_f16 v[30:33], a[216:219], v[248:251], v[30:33]
	v_mfma_f32_16x16x32_f16 v[30:33], a[220:223], v[252:255], v[30:33]
	ds_write_b128 v174, v[14:17] offset:1024
	v_mfma_f32_16x16x32_f16 v[34:37], a[248:251], v[248:251], v[34:37]
	v_mfma_f32_16x16x32_f16 v[34:37], a[252:255], v[252:255], v[34:37]
	ds_write_b128 v174, v[18:21] offset:1536
	ds_write_b128 v174, v[22:25] offset:2048
	ds_write_b128 v174, v[26:29] offset:2560
	s_nop 1
	ds_write_b128 v174, v[30:33] offset:3072
	s_nop 1
	ds_write_b128 v174, v[34:37] offset:3584
	s_branch .Lwrites_done

.Lwrites_done:
	s_mov_b64 exec, -1
	s_waitcnt lgkmcnt(0)
	s_barrier
	ds_read_b128 v[2:5], v175
	ds_read_b128 v[224:227], v175 offset:4096
	ds_read_b128 v[228:231], v175 offset:8192
	ds_read_b128 v[232:235], v175 offset:12288
	s_mov_b64 exec, s[2:3]
	v_mov_b64_e32 v[6:7], 0
	v_mov_b64_e32 v[8:9], 0
	v_mov_b64_e32 v[10:11], 0
	v_mov_b64_e32 v[12:13], 0
	v_mov_b64_e32 v[14:15], 0
	v_mov_b64_e32 v[16:17], 0
	v_mov_b64_e32 v[18:19], 0
	v_mov_b64_e32 v[20:21], 0
	v_mov_b64_e32 v[22:23], 0
	v_mov_b64_e32 v[24:25], 0
	v_mov_b64_e32 v[26:27], 0
	v_mov_b64_e32 v[28:29], 0
	v_mov_b64_e32 v[30:31], 0
	v_mov_b64_e32 v[32:33], 0
	v_mov_b64_e32 v[34:35], 0
	v_mov_b64_e32 v[36:37], 0
	s_mov_b64 exec, -1
	s_waitcnt lgkmcnt(0)
	v_pk_add_f32 v[4:5], v[4:5], v[226:227]
	v_pk_add_f32 v[2:3], v[2:3], v[224:225]
	v_pk_add_f32 v[4:5], v[4:5], v[230:231]
	v_pk_add_f32 v[2:3], v[2:3], v[228:229]
	v_pk_add_f32 v[4:5], v[4:5], v[234:235]
	v_pk_add_f32 v[2:3], v[2:3], v[232:233]
	v_fma_f32 v4, v4, s37, v187
	v_fma_f32 v2, v2, s38, v185
	v_exp_f32_e32 v4, v4
	v_fma_f32 v3, v3, s38, v186
	v_exp_f32_e32 v2, v2
	v_fma_f32 v5, v5, s38, v188
	v_exp_f32_e32 v3, v3
	v_add_f32_e32 v4, 1.0, v4
	v_add_f32_e32 v2, 1.0, v2
	v_rcp_f32_e32 v4, v4
	v_rcp_f32_e32 v2, v2
	v_add_f32_e32 v3, 1.0, v3
	v_rcp_f32_e32 v3, v3
	v_exp_f32_e32 v5, v5
	v_fma_f32 v4, v4, -2.0, 1.0
	v_mul_f32_e32 v2, v2, v4
	v_add_f32_e32 v4, 1.0, v5
	v_fmac_f32_e32 v2, v177, v3
	v_rcp_f32_e32 v5, v4
	v_mul_f32_e32 v3, 0x4038aa3b, v2
	v_exp_f32_e32 v3, v3
	v_mov_b32_e32 v177, v2
	v_add_f32_e32 v3, 1.0, v3
	v_rcp_f32_e32 v3, v3
	s_nop 0
	v_fma_f32 v3, v3, -2.0, 1.0
	v_mul_f32_e32 v4, v5, v3
	v_fma_mixlo_f16 v3, v5, v3, 0
	v_and_b32_e32 v3, 0xffffbfff, v3
	v_or_b32_sdwa v108, s34, v3 dst_sel:DWORD dst_unused:UNUSED_PAD src0_sel:DWORD src1_sel:WORD_0
	s_nop 1
	v_mov_b32_dpp v109, v108 row_ror:8 row_mask:0xf bank_mask:0xf
	v_mov_b32_dpp v5, v4 row_ror:8 row_mask:0xf bank_mask:0xf
	s_and_saveexec_b64 s[12:13], s[0:1]
	v_lshl_or_b32 v108, v109, 16, v108
	s_andn2_b64 vcc, exec, s[4:5]
	s_cbranch_vccnz .Lpub_sc1
	buffer_store_dword v108, v176, s[8:11], 0 offen

.Lrestart3:
	s_and_b64 vcc, exec, s[6:7]
	s_cbranch_vccnz .Lfast3
	buffer_load_dwordx4 v[74:77], v78, s[8:11], s28 offen offset:3072 sc1
	s_add_i32 s17, s17, 1
	s_cmp_gt_u32 s17, 0x10000
	s_cselect_b64 s[6:7], -1, 0
	s_waitcnt vmcnt(0)
	v_bitop3_b32 v168, v74, v75, s30 bitop3:0x7e
	v_bitop3_b32 v169, v76, v77, s30 bitop3:0x7e
	v_bitop3_b32 v168, v168, v169, s18 bitop3:0xa8
	v_cmp_ne_u32_e32 vcc, 0, v168
	s_cbranch_vccnz .Lrestart3
	v_and_b32_e32 v248, v74, v167
	v_and_b32_e32 v249, v75, v167
	v_and_b32_e32 v250, v76, v167
	v_and_b32_e32 v251, v77, v167
	v_and_b32_dpp v252, v74, v167 row_ror:8 row_mask:0xf bank_mask:0xf
	v_and_b32_dpp v253, v75, v167 row_ror:8 row_mask:0xf bank_mask:0xf
	v_and_b32_dpp v254, v76, v167 row_ror:8 row_mask:0xf bank_mask:0xf
	v_and_b32_dpp v255, v77, v167 row_ror:8 row_mask:0xf bank_mask:0xf
	s_nop 0
	s_branch .Lfast3
